# GLA chunk loop: A^T build (D1) operand fragment pairs run up to four MFMAs ahead (idle registers, counted lgkmcnt waits) instead of one LDS round trip per two MFMAs
# baseline (speedup 1.0000x reference)
; #define LAS __attribute__((address_space(3)))
; __device__ __forceinline__ void gla_unit(LAS unsigned char* lds, const unsigned char* ws, const float* g_onorm, const int b, const int h, const int wv) {
;     ...
;         if (w < 3) {
;             const int st = (w == 2) ? 1 : 0, tt = (w == 0) ? 0 : 1;
;             f32x16 X;
; #pragma unroll
;             for (int r = 0; r < 16; ++r) X[r] = 0.f;
; #pragma unroll
;             for (int ks = 0; ks < 8; ++ks) {
;                 const bf16x8 ak = *(const LAS bf16x8*)(kb16 + 32 * st * QS + ks * 32);
;                 const bf16x8 bq2 = *(const LAS bf16x8*)(qb16 + 32 * tt * QS + ks * 32);
;                 X = __builtin_amdgcn_mfma_f32_32x32x16_bf16(ak, bq2, X, 0, 0, 0);
;             }
;             if (st == tt) {
; #pragma unroll
;                 for (int r = 0; r < 16; ++r) { const int sr = (r & 3) + 8 * (r >> 2) + 4 * hh; if (sr > j) X[r] = 0.f; }
;             }
.LBB0_642:
	v_cndmask_b32_e64 v64, 0, 1, s[54:55]
	v_cmp_ne_u32_e64 s[40:41], 1, v64
	v_cndmask_b32_e64 v64, 0, 1, s[62:63]
	s_andn2_b64 vcc, exec, s[54:55]
	v_add_u32_e32 v224, s61, v204
	v_add_u32_e32 v225, s64, v204
	v_cmp_ne_u32_e64 s[38:39], 1, v64
	s_cbranch_vccnz .LBB0_646
	ds_read_b128 v[64:67], v224 offset:17408
	ds_read_b128 v[68:71], v225
	ds_read_b128 v[80:83], v224 offset:17440
	ds_read_b128 v[84:87], v225 offset:32
	ds_read_b128 v[88:91], v224 offset:17472
	ds_read_b128 v[92:95], v225 offset:64
	ds_read_b128 v[228:231], v224 offset:17504
	ds_read_b128 v[232:235], v225 offset:96
	ds_read_b128 v[236:239], v224 offset:17536
	ds_read_b128 v[240:243], v225 offset:128
	s_and_b64 vcc, exec, s[38:39]
	s_waitcnt lgkmcnt(8)
	v_mfma_f32_32x32x16_bf16 v[64:79], v[64:67], v[68:71], 0
	s_waitcnt lgkmcnt(6)
	v_mfma_f32_32x32x16_bf16 v[64:79], v[80:83], v[84:87], v[64:79]
	ds_read_b128 v[80:83], v224 offset:17568
	ds_read_b128 v[84:87], v225 offset:160
	s_waitcnt lgkmcnt(6)
	v_mfma_f32_32x32x16_bf16 v[64:79], v[88:91], v[92:95], v[64:79]
	ds_read_b128 v[88:91], v224 offset:17600
	ds_read_b128 v[92:95], v225 offset:192
	s_waitcnt lgkmcnt(6)
	v_mfma_f32_32x32x16_bf16 v[64:79], v[228:231], v[232:235], v[64:79]
	ds_read_b128 v[228:231], v224 offset:17632
	ds_read_b128 v[232:235], v225 offset:224
	s_waitcnt lgkmcnt(6)
	v_mfma_f32_32x32x16_bf16 v[64:79], v[236:239], v[240:243], v[64:79]
	s_waitcnt lgkmcnt(4)
	v_mfma_f32_32x32x16_bf16 v[64:79], v[80:83], v[84:87], v[64:79]
	s_waitcnt lgkmcnt(2)
	v_mfma_f32_32x32x16_bf16 v[64:79], v[88:91], v[92:95], v[64:79]
	s_waitcnt lgkmcnt(0)
	v_mfma_f32_32x32x16_bf16 v[64:79], v[228:231], v[232:235], v[64:79]
	s_cbranch_vccnz .LBB0_645
	s_nop 10
	v_cndmask_b32_e64 v80, v64, 0, s[4:5]
	v_cndmask_b32_e64 v65, 0, v65, s[6:7]
	v_cndmask_b32_e64 v64, v80, v64, s[6:7]
	v_cndmask_b32_e64 v66, v66, 0, s[8:9]
	v_cndmask_b32_e64 v67, v67, 0, s[10:11]
	v_cndmask_b32_e64 v68, v68, 0, s[12:13]
	v_cndmask_b32_e64 v69, v69, 0, s[14:15]
	v_cndmask_b32_e64 v70, v70, 0, s[16:17]
	v_cndmask_b32_e64 v71, v71, 0, s[18:19]
	v_cndmask_b32_e64 v72, v72, 0, s[20:21]
	v_cndmask_b32_e64 v73, v73, 0, s[22:23]
	v_cndmask_b32_e64 v74, v74, 0, s[24:25]
	v_cndmask_b32_e64 v75, v75, 0, s[26:27]
	v_cndmask_b32_e64 v76, v76, 0, s[28:29]
	v_cndmask_b32_e64 v77, v77, 0, s[30:31]
	v_cndmask_b32_e64 v78, v78, 0, s[34:35]
	v_cndmask_b32_e64 v79, v79, 0, s[36:37]

; #define LAS __attribute__((address_space(3)))
; __device__ __forceinline__ void gla_unit(LAS unsigned char* lds, const unsigned char* ws, const float* g_onorm, const int b, const int h, const int wv) {
;     ...
;         if (w < 3) {
;             const int st = (w == 2) ? 1 : 0, tt = (w == 0) ? 0 : 1;
;             f32x16 X;
; #pragma unroll
;             for (int r = 0; r < 16; ++r) X[r] = 0.f;
; #pragma unroll
;             for (int ks = 0; ks < 8; ++ks) {
;                 const bf16x8 ak = *(const LAS bf16x8*)(kb16 + 32 * st * QS + ks * 32);
;                 const bf16x8 bq2 = *(const LAS bf16x8*)(qb16 + 32 * tt * QS + ks * 32);
;                 X = __builtin_amdgcn_mfma_f32_32x32x16_bf16(ak, bq2, X, 0, 0, 0);
;             }
;             if (st == tt) {
; #pragma unroll
;                 for (int r = 0; r < 16; ++r) { const int sr = (r & 3) + 8 * (r >> 2) + 4 * hh; if (sr > j) X[r] = 0.f; }
;             }
.LBB0_653:
	ds_read_b128 v[64:67], v224 offset:17408
	ds_read_b128 v[68:71], v225
	ds_read_b128 v[80:83], v224 offset:17440
	ds_read_b128 v[84:87], v225 offset:32
	ds_read_b128 v[88:91], v224 offset:17472
	ds_read_b128 v[92:95], v225 offset:64
	ds_read_b128 v[232:235], v224 offset:17504
	ds_read_b128 v[236:239], v225 offset:96
	ds_read_b128 v[240:243], v224 offset:17536
	ds_read_b128 v[248:251], v225 offset:128
	s_and_b64 vcc, exec, s[38:39]
	s_waitcnt lgkmcnt(8)
	v_mfma_f32_32x32x16_bf16 v[64:79], v[64:67], v[68:71], 0
	s_waitcnt lgkmcnt(6)
	v_mfma_f32_32x32x16_bf16 v[64:79], v[80:83], v[84:87], v[64:79]
	ds_read_b128 v[80:83], v224 offset:17568
	ds_read_b128 v[84:87], v225 offset:160
	s_waitcnt lgkmcnt(6)
	v_mfma_f32_32x32x16_bf16 v[64:79], v[88:91], v[92:95], v[64:79]
	ds_read_b128 v[88:91], v224 offset:17600
	ds_read_b128 v[92:95], v225 offset:192
	s_waitcnt lgkmcnt(6)
	v_mfma_f32_32x32x16_bf16 v[64:79], v[232:235], v[236:239], v[64:79]
	ds_read_b128 v[232:235], v224 offset:17632
	ds_read_b128 v[236:239], v225 offset:224
	s_waitcnt lgkmcnt(6)
	v_mfma_f32_32x32x16_bf16 v[64:79], v[240:243], v[248:251], v[64:79]
	s_waitcnt lgkmcnt(4)
	v_mfma_f32_32x32x16_bf16 v[64:79], v[80:83], v[84:87], v[64:79]
	s_waitcnt lgkmcnt(2)
	v_mfma_f32_32x32x16_bf16 v[64:79], v[88:91], v[92:95], v[64:79]
	s_waitcnt lgkmcnt(0)
	v_mfma_f32_32x32x16_bf16 v[64:79], v[232:235], v[236:239], v[64:79]
	s_cbranch_vccnz .LBB0_634
	s_nop 10
	v_cndmask_b32_e64 v80, v64, 0, s[4:5]
	v_cndmask_b32_e64 v65, 0, v65, s[6:7]
	v_cndmask_b32_e64 v64, v80, v64, s[6:7]
	v_cndmask_b32_e64 v66, v66, 0, s[8:9]
	v_cndmask_b32_e64 v67, v67, 0, s[10:11]
	v_cndmask_b32_e64 v68, v68, 0, s[12:13]
	v_cndmask_b32_e64 v69, v69, 0, s[14:15]
	v_cndmask_b32_e64 v70, v70, 0, s[16:17]
	v_cndmask_b32_e64 v71, v71, 0, s[18:19]
	v_cndmask_b32_e64 v72, v72, 0, s[20:21]
	v_cndmask_b32_e64 v73, v73, 0, s[22:23]
	v_cndmask_b32_e64 v74, v74, 0, s[24:25]
	v_cndmask_b32_e64 v75, v75, 0, s[26:27]
	v_cndmask_b32_e64 v76, v76, 0, s[28:29]
	v_cndmask_b32_e64 v77, v77, 0, s[30:31]
	v_cndmask_b32_e64 v78, v78, 0, s[34:35]
	v_cndmask_b32_e64 v79, v79, 0, s[36:37]
	s_branch .LBB0_634

; #define LAS __attribute__((address_space(3)))
; __device__ __forceinline__ void gla_unit(LAS unsigned char* lds, const unsigned char* ws, const float* g_onorm, const int b, const int h, const int wv) {
;     ...
;         if (w < 3) {
;             const int st = (w == 2) ? 1 : 0, tt = (w == 0) ? 0 : 1;
;             f32x16 X;
; #pragma unroll
;             for (int r = 0; r < 16; ++r) X[r] = 0.f;
; #pragma unroll
;             for (int ks = 0; ks < 8; ++ks) {
;                 const bf16x8 ak = *(const LAS bf16x8*)(kb16 + 32 * st * QS + ks * 32);
;                 const bf16x8 bq2 = *(const LAS bf16x8*)(qb16 + 32 * tt * QS + ks * 32);
;                 X = __builtin_amdgcn_mfma_f32_32x32x16_bf16(ak, bq2, X, 0, 0, 0);
;             }
;             if (st == tt) {
; #pragma unroll
;                 for (int r = 0; r < 16; ++r) { const int sr = (r & 3) + 8 * (r >> 2) + 4 * hh; if (sr > j) X[r] = 0.f; }
;             }
.LBB0_1699:
	v_cndmask_b32_e64 v64, 0, 1, s[46:47]
	v_cmp_ne_u32_e64 s[40:41], 1, v64
	v_cndmask_b32_e64 v64, 0, 1, s[48:49]
	s_andn2_b64 vcc, exec, s[46:47]
	v_add_u32_e32 v224, s67, v204
	v_add_u32_e32 v225, s70, v204
	v_cmp_ne_u32_e64 s[38:39], 1, v64
	s_cbranch_vccnz .LBB0_1703
	ds_read_b128 v[64:67], v224 offset:17408
	ds_read_b128 v[68:71], v225
	ds_read_b128 v[80:83], v224 offset:17440
	ds_read_b128 v[84:87], v225 offset:32
	ds_read_b128 v[88:91], v224 offset:17472
	ds_read_b128 v[92:95], v225 offset:64
	ds_read_b128 v[228:231], v224 offset:17504
	ds_read_b128 v[232:235], v225 offset:96
	ds_read_b128 v[236:239], v224 offset:17536
	ds_read_b128 v[240:243], v225 offset:128
	s_and_b64 vcc, exec, s[38:39]
	s_waitcnt lgkmcnt(8)
	v_mfma_f32_32x32x16_bf16 v[64:79], v[64:67], v[68:71], 0
	s_waitcnt lgkmcnt(6)
	v_mfma_f32_32x32x16_bf16 v[64:79], v[80:83], v[84:87], v[64:79]
	ds_read_b128 v[80:83], v224 offset:17568
	ds_read_b128 v[84:87], v225 offset:160
	s_waitcnt lgkmcnt(6)
	v_mfma_f32_32x32x16_bf16 v[64:79], v[88:91], v[92:95], v[64:79]
	ds_read_b128 v[88:91], v224 offset:17600
	ds_read_b128 v[92:95], v225 offset:192
	s_waitcnt lgkmcnt(6)
	v_mfma_f32_32x32x16_bf16 v[64:79], v[228:231], v[232:235], v[64:79]
	ds_read_b128 v[228:231], v224 offset:17632
	ds_read_b128 v[232:235], v225 offset:224
	s_waitcnt lgkmcnt(6)
	v_mfma_f32_32x32x16_bf16 v[64:79], v[236:239], v[240:243], v[64:79]
	s_waitcnt lgkmcnt(4)
	v_mfma_f32_32x32x16_bf16 v[64:79], v[80:83], v[84:87], v[64:79]
	s_waitcnt lgkmcnt(2)
	v_mfma_f32_32x32x16_bf16 v[64:79], v[88:91], v[92:95], v[64:79]
	s_waitcnt lgkmcnt(0)
	v_mfma_f32_32x32x16_bf16 v[64:79], v[228:231], v[232:235], v[64:79]
	s_cbranch_vccnz .LBB0_1702
	s_nop 10
	v_cndmask_b32_e64 v80, v64, 0, s[4:5]
	v_cndmask_b32_e64 v65, 0, v65, s[6:7]
	v_cndmask_b32_e64 v64, v80, v64, s[6:7]
	v_cndmask_b32_e64 v66, v66, 0, s[8:9]
	v_cndmask_b32_e64 v67, v67, 0, s[10:11]
	v_cndmask_b32_e64 v68, v68, 0, s[12:13]
	v_cndmask_b32_e64 v69, v69, 0, s[14:15]
	v_cndmask_b32_e64 v70, v70, 0, s[16:17]
	v_cndmask_b32_e64 v71, v71, 0, s[18:19]
	v_cndmask_b32_e64 v72, v72, 0, s[20:21]
	v_cndmask_b32_e64 v73, v73, 0, s[22:23]
	v_cndmask_b32_e64 v74, v74, 0, s[24:25]
	v_cndmask_b32_e64 v75, v75, 0, s[26:27]
	v_cndmask_b32_e64 v76, v76, 0, s[28:29]
	v_cndmask_b32_e64 v77, v77, 0, s[30:31]
	v_cndmask_b32_e64 v78, v78, 0, s[34:35]
	v_cndmask_b32_e64 v79, v79, 0, s[36:37]
